# T2 LoRA input pass: one activation sequence per element with per-lane constants (tanh | identity | sigmoid by lane) instead of both exec-masked sequences; same IEEE division with the numerator in a VG
# speedup vs baseline: 1.0077x; 1.0004x over previous
; __device__ __forceinline__ int lane_id() { int l; asm volatile("v_mbcnt_lo_u32_b32 %0, -1, 0\n\tv_mbcnt_hi_u32_b32 %0, -1, %0" : "=v"(l)); return l; }
; __device__ __forceinline__ float sigmoidf_(float x) { return 1.f / (1.f + __expf(-x)); }
; __device__ __forceinline__ void rwkv_lin_ph(const int WID_, const bf16* __restrict__ proj, const float* __restrict__ mu, bf16* __restrict__ lin, const int row_lo, const int row_hi) {
;     const int lane = lane_id(), wv = WID_;
;     const float4 m4 = *(const float4*)(mu + 1536 + 4 * lane);
;     const float mm[4] = {m4.x, m4.y, m4.z, m4.w};
;     for (int m0 = row_lo + wv * 4; m0 < row_hi; m0 += 32) {
;         uint2 z[4], zp[4];
; #pragma unroll
;         for (int i = 0; i < 4; ++i) { const int m = m0 + i; z[i] = *(const uint2*)(proj + (size_t)m * DSHIFT + 1536 + 4 * lane);
;             zp[i] = make_uint2(0, 0); if ((m & (S - 1)) != 0) zp[i] = *(const uint2*)(proj + (size_t)(m - 1) * DSHIFT + 1536 + 4 * lane); }
; #pragma unroll
;         for (int i = 0; i < 4; ++i) {
;             float c[4] = {__builtin_bit_cast(float, z[i].x << 16), __builtin_bit_cast(float, z[i].x & 0xffff0000u), __builtin_bit_cast(float, z[i].y << 16), __builtin_bit_cast(float, z[i].y & 0xffff0000u)};
;             const float q[4] = {__builtin_bit_cast(float, zp[i].x << 16), __builtin_bit_cast(float, zp[i].x & 0xffff0000u), __builtin_bit_cast(float, zp[i].y << 16), __builtin_bit_cast(float, zp[i].y & 0xffff0000u)};
; #pragma unroll
;             for (int e = 0; e < 4; ++e) { float t = c[e] + (q[e] - c[e]) * mm[e];
;                 if (lane < 16) t = 1.f - 2.f / (1.f + __expf(2.f * t));
;                 else if (lane >= 32) t = sigmoidf_(t);
.LBB0_449:
	v_readlane_b32 s0, v243, 55
	v_readlane_b32 s1, v243, 56
	s_andn2_b64 vcc, exec, s[0:1]
	v_mbcnt_lo_u32_b32 v4, -1, 0
	v_mbcnt_hi_u32_b32 v4, -1, v4
	s_cbranch_vccnz .LBB0_551
	v_lshlrev_b32_e32 v6, 2, v4
	v_ashrrev_i32_e32 v7, 31, v6
	v_lshl_add_u64 v[0:1], v[6:7], 2, s[74:75]
	global_load_dwordx4 v[0:3], v[0:1], off
	s_ashr_i32 s37, s36, 31
	s_lshl_b64 s[0:1], s[36:37], 9
	s_add_u32 s4, s92, s0
	s_addc_u32 s5, s93, s1
	s_mul_i32 s1, s36, 0xe00
	s_mul_hi_i32 s0, s36, 0xe00
	s_add_u32 s18, s82, s1
	s_addc_u32 s19, s80, s0
	s_ashr_i32 s39, s38, 31
	s_lshl_b64 s[0:1], s[38:39], 9
	s_add_u32 s44, s92, s0
	s_addc_u32 s45, s93, s1
	s_mul_i32 s1, s38, 0xe00
	s_mul_hi_i32 s0, s38, 0xe00
	s_add_u32 s46, s82, s1
	s_addc_u32 s47, s80, s0
	s_ashr_i32 s41, s40, 31
	s_lshl_b64 s[0:1], s[40:41], 9
	s_add_u32 s48, s92, s0
	s_addc_u32 s49, s93, s1
	s_mul_i32 s1, s40, 0xe00
	s_mul_hi_i32 s0, s40, 0xe00
	s_add_u32 s50, s82, s1
	s_addc_u32 s51, s80, s0
	s_ashr_i32 s35, s34, 31
	s_lshl_b64 s[0:1], s[34:35], 9
	s_add_u32 s52, s92, s0
	s_addc_u32 s53, s93, s1
	s_mul_i32 s1, s34, 0xe00
	s_mul_hi_i32 s0, s34, 0xe00
	s_add_u32 s60, s82, s1
	s_addc_u32 s61, s80, s0
	s_lshl_b32 s6, s7, 8
	v_cmp_lt_i32_e64 s[0:1], 15, v4
	v_cmp_lt_u32_e64 s[2:3], 31, v4
	v_lshlrev_b64 v[4:5], 1, v[6:7]
	s_or_b32 s6, s6, 0xe0
	v_lshl_add_u64 v[6:7], s[92:93], 0, v[4:5]
	s_nop 3
	s_andn2_b64 s[98:99], s[0:1], s[2:3]
	v_mov_b32_e32 v27, 0xbfb8aa3b
	v_mov_b32_e32 v28, 0x4038aa3b
	v_cndmask_b32_e64 v27, v28, v27, s[0:1]
	v_mov_b32_e32 v28, 2.0
	v_cndmask_b32_e64 v28, v28, 1.0, s[0:1]
	s_mov_b32 s10, s83
	s_branch .LBB0_452

; __device__ __forceinline__ unsigned pk2(float lo, float hi) { const f32x2h v = {lo, hi}; const bf16x2h b = __builtin_convertvector(v, bf16x2h); return __builtin_bit_cast(unsigned, b); }
; __device__ __forceinline__ float sigmoidf_(float x) { return 1.f / (1.f + __expf(-x)); }
; __device__ __forceinline__ void rwkv_lin_ph(const int WID_, const bf16* __restrict__ proj, const float* __restrict__ mu, bf16* __restrict__ lin, const int row_lo, const int row_hi) {
;     ...
;         for (int i = 0; i < 4; ++i) { const int m = m0 + i; z[i] = *(const uint2*)(proj + (size_t)m * DSHIFT + 1536 + 4 * lane);
;             zp[i] = make_uint2(0, 0); if ((m & (S - 1)) != 0) zp[i] = *(const uint2*)(proj + (size_t)(m - 1) * DSHIFT + 1536 + 4 * lane); }
; #pragma unroll
;         for (int i = 0; i < 4; ++i) {
;             float c[4] = {__builtin_bit_cast(float, z[i].x << 16), __builtin_bit_cast(float, z[i].x & 0xffff0000u), __builtin_bit_cast(float, z[i].y << 16), __builtin_bit_cast(float, z[i].y & 0xffff0000u)};
;             const float q[4] = {__builtin_bit_cast(float, zp[i].x << 16), __builtin_bit_cast(float, zp[i].x & 0xffff0000u), __builtin_bit_cast(float, zp[i].y << 16), __builtin_bit_cast(float, zp[i].y & 0xffff0000u)};
; #pragma unroll
;             for (int e = 0; e < 4; ++e) { float t = c[e] + (q[e] - c[e]) * mm[e];
;                 if (lane < 16) t = 1.f - 2.f / (1.f + __expf(2.f * t));
;                 else if (lane >= 32) t = sigmoidf_(t);
;                 c[e] = t; }
;             uint2 o; o.x = pk2(c[0], c[1]); o.y = pk2(c[2], c[3]);
;             *(uint2*)(lin + (size_t)(m0 + i) * 256 + 4 * lane) = o;
.LBB0_455:
	v_lshl_add_u64 v[8:9], s[50:51], 0, v[4:5]
	global_load_dwordx2 v[12:13], v[8:9], off
	v_lshl_add_u64 v[8:9], s[46:47], 0, v[4:5]
	global_load_dwordx2 v[10:11], v[8:9], off
	v_lshl_add_u64 v[8:9], s[18:19], 0, v[4:5]
	global_load_dwordx2 v[8:9], v[8:9], off
	s_waitcnt vmcnt(0)
	v_lshlrev_b32_e32 v18, 16, v14
	v_lshlrev_b32_e32 v19, 16, v16
	v_sub_f32_e32 v19, v19, v18
	v_fma_f32 v19, v0, v19, v18
	v_mul_f32_e32 v29, v27, v19
	v_exp_f32_e32 v29, v29
	s_nop 0
	v_add_f32_e32 v29, 1.0, v29
	v_div_scale_f32 v30, s[10:11], v29, v29, v28
	v_rcp_f32_e32 v31, v30
	v_div_scale_f32 v32, vcc, v28, v29, v28
	v_fma_f32 v33, -v30, v31, 1.0
	v_fmac_f32_e32 v31, v33, v31
	v_mul_f32_e32 v33, v32, v31
	v_fma_f32 v34, -v30, v33, v32
	v_fmac_f32_e32 v33, v34, v31
	v_fma_f32 v30, -v30, v33, v32
	v_div_fmas_f32 v30, v30, v31, v33
	v_div_fixup_f32 v29, v30, v29, v28
	v_sub_f32_e32 v30, 1.0, v29
	v_cndmask_b32_e64 v29, v30, v29, s[0:1]
	v_cndmask_b32_e64 v19, v29, v19, s[98:99]
	v_and_b32_e32 v14, 0xffff0000, v14
	v_and_b32_e32 v16, 0xffff0000, v16
	v_sub_f32_e32 v16, v16, v14
	v_fma_f32 v20, v1, v16, v14
	v_mul_f32_e32 v29, v27, v20
	v_exp_f32_e32 v29, v29
	s_nop 0
	v_add_f32_e32 v29, 1.0, v29
	v_div_scale_f32 v30, s[10:11], v29, v29, v28
	v_rcp_f32_e32 v31, v30
	v_div_scale_f32 v32, vcc, v28, v29, v28
	v_fma_f32 v33, -v30, v31, 1.0
	v_fmac_f32_e32 v31, v33, v31
	v_mul_f32_e32 v33, v32, v31
	v_fma_f32 v34, -v30, v33, v32
	v_fmac_f32_e32 v33, v34, v31
	v_fma_f32 v30, -v30, v33, v32
	v_div_fmas_f32 v30, v30, v31, v33
	v_div_fixup_f32 v29, v30, v29, v28
	v_sub_f32_e32 v30, 1.0, v29
	v_cndmask_b32_e64 v29, v30, v29, s[0:1]
	v_cndmask_b32_e64 v20, v29, v20, s[98:99]
	v_lshlrev_b32_e32 v16, 16, v15
	v_lshlrev_b32_e32 v21, 16, v17
	v_sub_f32_e32 v21, v21, v16
	v_fma_f32 v21, v2, v21, v16
	v_mul_f32_e32 v29, v27, v21
	v_exp_f32_e32 v29, v29
	s_nop 0
	v_add_f32_e32 v29, 1.0, v29
	v_div_scale_f32 v30, s[10:11], v29, v29, v28
	v_rcp_f32_e32 v31, v30
	v_div_scale_f32 v32, vcc, v28, v29, v28
	v_fma_f32 v33, -v30, v31, 1.0
	v_fmac_f32_e32 v31, v33, v31
	v_mul_f32_e32 v33, v32, v31
	v_fma_f32 v34, -v30, v33, v32
	v_fmac_f32_e32 v33, v34, v31
	v_fma_f32 v30, -v30, v33, v32
	v_div_fmas_f32 v30, v30, v31, v33
	v_div_fixup_f32 v29, v30, v29, v28
	v_sub_f32_e32 v30, 1.0, v29
	v_cndmask_b32_e64 v29, v30, v29, s[0:1]
	v_cndmask_b32_e64 v21, v29, v21, s[98:99]
	v_and_b32_e32 v15, 0xffff0000, v15
	v_and_b32_e32 v17, 0xffff0000, v17
	v_sub_f32_e32 v17, v17, v15
	v_fma_f32 v17, v3, v17, v15
	v_mul_f32_e32 v29, v27, v17
	v_exp_f32_e32 v29, v29
	s_nop 0
	v_add_f32_e32 v29, 1.0, v29
	v_div_scale_f32 v30, s[10:11], v29, v29, v28
	v_rcp_f32_e32 v31, v30
	v_div_scale_f32 v32, vcc, v28, v29, v28
	v_fma_f32 v33, -v30, v31, 1.0
	v_fmac_f32_e32 v31, v33, v31
	v_mul_f32_e32 v33, v32, v31
	v_fma_f32 v34, -v30, v33, v32
	v_fmac_f32_e32 v33, v34, v31
	v_fma_f32 v30, -v30, v33, v32
	v_div_fmas_f32 v30, v30, v31, v33
	v_div_fixup_f32 v29, v30, v29, v28
	v_sub_f32_e32 v30, 1.0, v29
	v_cndmask_b32_e64 v29, v30, v29, s[0:1]
	v_cndmask_b32_e64 v17, v29, v17, s[98:99]
	v_cvt_pk_bf16_f32 v21, v21, v17
	v_lshl_add_u64 v[22:23], s[52:53], 0, v[4:5]
	v_lshlrev_b32_e32 v17, 16, v12
	v_add_co_u32_e32 v22, vcc, 0x23000000, v22
	v_sub_f32_e32 v18, v18, v17
	v_cvt_pk_bf16_f32 v20, v19, v20
	v_addc_co_u32_e32 v23, vcc, 0, v23, vcc
	v_fma_f32 v18, v0, v18, v17
	global_store_dwordx2 v[22:23], v[20:21], off
	v_mul_f32_e32 v29, v27, v18
	v_exp_f32_e32 v29, v29
	s_nop 0
	v_add_f32_e32 v29, 1.0, v29
	v_div_scale_f32 v30, s[10:11], v29, v29, v28
	v_rcp_f32_e32 v31, v30
	v_div_scale_f32 v32, vcc, v28, v29, v28
	v_fma_f32 v33, -v30, v31, 1.0
	v_fmac_f32_e32 v31, v33, v31
	v_mul_f32_e32 v33, v32, v31
	v_fma_f32 v34, -v30, v33, v32
	v_fmac_f32_e32 v33, v34, v31
	v_fma_f32 v30, -v30, v33, v32
	v_div_fmas_f32 v30, v30, v31, v33
	v_div_fixup_f32 v29, v30, v29, v28
	v_sub_f32_e32 v30, 1.0, v29
	v_cndmask_b32_e64 v29, v30, v29, s[0:1]
	v_cndmask_b32_e64 v18, v29, v18, s[98:99]
	v_and_b32_e32 v12, 0xffff0000, v12
	v_sub_f32_e32 v14, v14, v12
	v_fma_f32 v19, v1, v14, v12
	v_mul_f32_e32 v29, v27, v19
	v_exp_f32_e32 v29, v29
	s_nop 0
	v_add_f32_e32 v29, 1.0, v29
	v_div_scale_f32 v30, s[10:11], v29, v29, v28
	v_rcp_f32_e32 v31, v30
	v_div_scale_f32 v32, vcc, v28, v29, v28
	v_fma_f32 v33, -v30, v31, 1.0
	v_fmac_f32_e32 v31, v33, v31
	v_mul_f32_e32 v33, v32, v31
	v_fma_f32 v34, -v30, v33, v32
	v_fmac_f32_e32 v33, v34, v31
	v_fma_f32 v30, -v30, v33, v32
	v_div_fmas_f32 v30, v30, v31, v33
	v_div_fixup_f32 v29, v30, v29, v28
	v_sub_f32_e32 v30, 1.0, v29
	v_cndmask_b32_e64 v29, v30, v29, s[0:1]
	v_cndmask_b32_e64 v19, v29, v19, s[98:99]
	v_lshlrev_b32_e32 v14, 16, v13
	v_sub_f32_e32 v16, v16, v14
	v_fma_f32 v20, v2, v16, v14
	v_mul_f32_e32 v29, v27, v20
	v_exp_f32_e32 v29, v29
	s_nop 0
	v_add_f32_e32 v29, 1.0, v29
	v_div_scale_f32 v30, s[10:11], v29, v29, v28
	v_rcp_f32_e32 v31, v30
	v_div_scale_f32 v32, vcc, v28, v29, v28
	v_fma_f32 v33, -v30, v31, 1.0
	v_fmac_f32_e32 v31, v33, v31
	v_mul_f32_e32 v33, v32, v31
	v_fma_f32 v34, -v30, v33, v32
	v_fmac_f32_e32 v33, v34, v31
	v_fma_f32 v30, -v30, v33, v32
	v_div_fmas_f32 v30, v30, v31, v33
	v_div_fixup_f32 v29, v30, v29, v28
	v_sub_f32_e32 v30, 1.0, v29
	v_cndmask_b32_e64 v29, v30, v29, s[0:1]
	v_cndmask_b32_e64 v20, v29, v20, s[98:99]
	v_and_b32_e32 v16, 0xffff0000, v13
	v_sub_f32_e32 v13, v15, v16
	v_fma_f32 v13, v3, v13, v16
	v_mul_f32_e32 v29, v27, v13
	v_exp_f32_e32 v29, v29
	s_nop 0
	v_add_f32_e32 v29, 1.0, v29
	v_div_scale_f32 v30, s[10:11], v29, v29, v28
	v_rcp_f32_e32 v31, v30
	v_div_scale_f32 v32, vcc, v28, v29, v28
	v_fma_f32 v33, -v30, v31, 1.0
	v_fmac_f32_e32 v31, v33, v31
; __device__ __forceinline__ unsigned pk2(float lo, float hi) { const f32x2h v = {lo, hi}; const bf16x2h b = __builtin_convertvector(v, bf16x2h); return __builtin_bit_cast(unsigned, b); }
; __device__ __forceinline__ float sigmoidf_(float x) { return 1.f / (1.f + __expf(-x)); }
; __device__ __forceinline__ void rwkv_lin_ph(const int WID_, const bf16* __restrict__ proj, const float* __restrict__ mu, bf16* __restrict__ lin, const int row_lo, const int row_hi) {
;     ...
;         for (int i = 0; i < 4; ++i) { const int m = m0 + i; z[i] = *(const uint2*)(proj + (size_t)m * DSHIFT + 1536 + 4 * lane);
;             zp[i] = make_uint2(0, 0); if ((m & (S - 1)) != 0) zp[i] = *(const uint2*)(proj + (size_t)(m - 1) * DSHIFT + 1536 + 4 * lane); }
; #pragma unroll
;         for (int i = 0; i < 4; ++i) {
;             float c[4] = {__builtin_bit_cast(float, z[i].x << 16), __builtin_bit_cast(float, z[i].x & 0xffff0000u), __builtin_bit_cast(float, z[i].y << 16), __builtin_bit_cast(float, z[i].y & 0xffff0000u)};
;             const float q[4] = {__builtin_bit_cast(float, zp[i].x << 16), __builtin_bit_cast(float, zp[i].x & 0xffff0000u), __builtin_bit_cast(float, zp[i].y << 16), __builtin_bit_cast(float, zp[i].y & 0xffff0000u)};
; #pragma unroll
;             for (int e = 0; e < 4; ++e) { float t = c[e] + (q[e] - c[e]) * mm[e];
;                 if (lane < 16) t = 1.f - 2.f / (1.f + __expf(2.f * t));
;                 else if (lane >= 32) t = sigmoidf_(t);
;                 c[e] = t; }
;             uint2 o; o.x = pk2(c[0], c[1]); o.y = pk2(c[2], c[3]);
;             *(uint2*)(lin + (size_t)(m0 + i) * 256 + 4 * lane) = o;
	v_mul_f32_e32 v33, v32, v31
	v_fma_f32 v34, -v30, v33, v32
	v_fmac_f32_e32 v33, v34, v31
	v_fma_f32 v30, -v30, v33, v32
	v_div_fmas_f32 v30, v30, v31, v33
	v_div_fixup_f32 v29, v30, v29, v28
	v_sub_f32_e32 v30, 1.0, v29
	v_cndmask_b32_e64 v29, v30, v29, s[0:1]
	v_cndmask_b32_e64 v13, v29, v13, s[98:99]
	v_cvt_pk_bf16_f32 v18, v18, v19
	v_cvt_pk_bf16_f32 v19, v20, v13
	v_lshl_add_u64 v[20:21], s[48:49], 0, v[4:5]
	v_lshlrev_b32_e32 v15, 16, v10
	v_add_co_u32_e32 v20, vcc, 0x23000000, v20
	v_sub_f32_e32 v13, v17, v15
	s_nop 0
	v_addc_co_u32_e32 v21, vcc, 0, v21, vcc
	v_fma_f32 v17, v0, v13, v15
	global_store_dwordx2 v[20:21], v[18:19], off
	v_mul_f32_e32 v29, v27, v17
	v_exp_f32_e32 v29, v29
	s_nop 0
	v_add_f32_e32 v29, 1.0, v29
	v_div_scale_f32 v30, s[10:11], v29, v29, v28
	v_rcp_f32_e32 v31, v30
	v_div_scale_f32 v32, vcc, v28, v29, v28
	v_fma_f32 v33, -v30, v31, 1.0
	v_fmac_f32_e32 v31, v33, v31
	v_mul_f32_e32 v33, v32, v31
	v_fma_f32 v34, -v30, v33, v32
	v_fmac_f32_e32 v33, v34, v31
	v_fma_f32 v30, -v30, v33, v32
	v_div_fmas_f32 v30, v30, v31, v33
	v_div_fixup_f32 v29, v30, v29, v28
	v_sub_f32_e32 v30, 1.0, v29
	v_cndmask_b32_e64 v29, v30, v29, s[0:1]
	v_cndmask_b32_e64 v17, v29, v17, s[98:99]
	v_and_b32_e32 v13, 0xffff0000, v10
	v_sub_f32_e32 v10, v12, v13
	v_fma_f32 v18, v1, v10, v13
	v_mul_f32_e32 v29, v27, v18
	v_exp_f32_e32 v29, v29
	s_nop 0
	v_add_f32_e32 v29, 1.0, v29
	v_div_scale_f32 v30, s[10:11], v29, v29, v28
	v_rcp_f32_e32 v31, v30
	v_div_scale_f32 v32, vcc, v28, v29, v28
	v_fma_f32 v33, -v30, v31, 1.0
	v_fmac_f32_e32 v31, v33, v31
	v_mul_f32_e32 v33, v32, v31
	v_fma_f32 v34, -v30, v33, v32
	v_fmac_f32_e32 v33, v34, v31
	v_fma_f32 v30, -v30, v33, v32
	v_div_fmas_f32 v30, v30, v31, v33
	v_div_fixup_f32 v29, v30, v29, v28
	v_sub_f32_e32 v30, 1.0, v29
	v_cndmask_b32_e64 v29, v30, v29, s[0:1]
	v_cndmask_b32_e64 v18, v29, v18, s[98:99]
	v_lshlrev_b32_e32 v12, 16, v11
	v_sub_f32_e32 v10, v14, v12
	v_fma_f32 v14, v2, v10, v12
	v_mul_f32_e32 v29, v27, v14
	v_exp_f32_e32 v29, v29
	s_nop 0
	v_add_f32_e32 v29, 1.0, v29
	v_div_scale_f32 v30, s[10:11], v29, v29, v28
	v_rcp_f32_e32 v31, v30
	v_div_scale_f32 v32, vcc, v28, v29, v28
	v_fma_f32 v33, -v30, v31, 1.0
	v_fmac_f32_e32 v31, v33, v31
	v_mul_f32_e32 v33, v32, v31
	v_fma_f32 v34, -v30, v33, v32
	v_fmac_f32_e32 v33, v34, v31
	v_fma_f32 v30, -v30, v33, v32
	v_div_fmas_f32 v30, v30, v31, v33
	v_div_fixup_f32 v29, v30, v29, v28
	v_sub_f32_e32 v30, 1.0, v29
	v_cndmask_b32_e64 v29, v30, v29, s[0:1]
	v_cndmask_b32_e64 v14, v29, v14, s[98:99]
	v_and_b32_e32 v10, 0xffff0000, v11
	v_sub_f32_e32 v11, v16, v10
	v_fma_f32 v11, v3, v11, v10
	v_mul_f32_e32 v29, v27, v11
	v_exp_f32_e32 v29, v29
	s_nop 0
	v_add_f32_e32 v29, 1.0, v29
	v_div_scale_f32 v30, s[10:11], v29, v29, v28
	v_rcp_f32_e32 v31, v30
	v_div_scale_f32 v32, vcc, v28, v29, v28
	v_fma_f32 v33, -v30, v31, 1.0
	v_fmac_f32_e32 v31, v33, v31
	v_mul_f32_e32 v33, v32, v31
	v_fma_f32 v34, -v30, v33, v32
	v_fmac_f32_e32 v33, v34, v31
	v_fma_f32 v30, -v30, v33, v32
	v_div_fmas_f32 v30, v30, v31, v33
	v_div_fixup_f32 v29, v30, v29, v28
	v_sub_f32_e32 v30, 1.0, v29
	v_cndmask_b32_e64 v29, v30, v29, s[0:1]
	v_cndmask_b32_e64 v11, v29, v11, s[98:99]
	v_cvt_pk_bf16_f32 v16, v17, v18
	v_cvt_pk_bf16_f32 v17, v14, v11
	v_lshl_add_u64 v[18:19], s[44:45], 0, v[4:5]
	v_lshlrev_b32_e32 v11, 16, v8
	v_add_co_u32_e32 v18, vcc, 0x23000000, v18
	v_sub_f32_e32 v14, v15, v11
	s_nop 0
	v_addc_co_u32_e32 v19, vcc, 0, v19, vcc
	v_fmac_f32_e32 v11, v0, v14
	global_store_dwordx2 v[18:19], v[16:17], off
	v_mul_f32_e32 v29, v27, v11
	v_exp_f32_e32 v29, v29
	s_nop 0
	v_add_f32_e32 v29, 1.0, v29
	v_div_scale_f32 v30, s[10:11], v29, v29, v28
	v_rcp_f32_e32 v31, v30
	v_div_scale_f32 v32, vcc, v28, v29, v28
	v_fma_f32 v33, -v30, v31, 1.0
	v_fmac_f32_e32 v31, v33, v31
	v_mul_f32_e32 v33, v32, v31
	v_fma_f32 v34, -v30, v33, v32
	v_fmac_f32_e32 v33, v34, v31
	v_fma_f32 v30, -v30, v33, v32
	v_div_fmas_f32 v30, v30, v31, v33
	v_div_fixup_f32 v29, v30, v29, v28
	v_sub_f32_e32 v30, 1.0, v29
	v_cndmask_b32_e64 v29, v30, v29, s[0:1]
	v_cndmask_b32_e64 v11, v29, v11, s[98:99]
	v_and_b32_e32 v8, 0xffff0000, v8
	v_sub_f32_e32 v13, v13, v8
	v_fmac_f32_e32 v8, v1, v13
	v_mul_f32_e32 v29, v27, v8
	v_exp_f32_e32 v29, v29
	s_nop 0
	v_add_f32_e32 v29, 1.0, v29
	v_div_scale_f32 v30, s[10:11], v29, v29, v28
	v_rcp_f32_e32 v31, v30
	v_div_scale_f32 v32, vcc, v28, v29, v28
	v_fma_f32 v33, -v30, v31, 1.0
	v_fmac_f32_e32 v31, v33, v31
	v_mul_f32_e32 v33, v32, v31
	v_fma_f32 v34, -v30, v33, v32
	v_fmac_f32_e32 v33, v34, v31
	v_fma_f32 v30, -v30, v33, v32
	v_div_fmas_f32 v30, v30, v31, v33
	v_div_fixup_f32 v29, v30, v29, v28
	v_sub_f32_e32 v30, 1.0, v29
	v_cndmask_b32_e64 v29, v30, v29, s[0:1]
	v_cndmask_b32_e64 v8, v29, v8, s[98:99]
	v_lshlrev_b32_e32 v13, 16, v9
	v_sub_f32_e32 v12, v12, v13
	v_fmac_f32_e32 v13, v2, v12
	v_mul_f32_e32 v29, v27, v13
	v_exp_f32_e32 v29, v29
	s_nop 0
	v_add_f32_e32 v29, 1.0, v29
	v_div_scale_f32 v30, s[10:11], v29, v29, v28
	v_rcp_f32_e32 v31, v30
	v_div_scale_f32 v32, vcc, v28, v29, v28
	v_fma_f32 v33, -v30, v31, 1.0
	v_fmac_f32_e32 v31, v33, v31
	v_mul_f32_e32 v33, v32, v31
	v_fma_f32 v34, -v30, v33, v32
	v_fmac_f32_e32 v33, v34, v31
	v_fma_f32 v30, -v30, v33, v32
	v_div_fmas_f32 v30, v30, v31, v33
	v_div_fixup_f32 v29, v30, v29, v28
	v_sub_f32_e32 v30, 1.0, v29
	v_cndmask_b32_e64 v29, v30, v29, s[0:1]
	v_cndmask_b32_e64 v13, v29, v13, s[98:99]
	v_and_b32_e32 v9, 0xffff0000, v9
	v_sub_f32_e32 v10, v10, v9
	v_fmac_f32_e32 v9, v3, v10
	s_and_saveexec_b64 s[10:11], s[0:1]
	s_xor_b64 s[62:63], exec, s[10:11]
	s_cbranch_execz .LBB0_549
	s_and_saveexec_b64 s[68:69], s[2:3]
	s_cbranch_execz .LBB0_548
	v_mul_f32_e32 v9, 0xbfb8aa3b, v9
	v_exp_f32_e32 v9, v9
	s_nop 0
	v_add_f32_e32 v9, 1.0, v9
	v_div_scale_f32 v10, s[10:11], v9, v9, 1.0
	v_rcp_f32_e32 v12, v10
	v_div_scale_f32 v14, vcc, 1.0, v9, 1.0
	v_fma_f32 v15, -v10, v12, 1.0
	v_fmac_f32_e32 v12, v15, v12
	v_mul_f32_e32 v15, v14, v12
	v_fma_f32 v16, -v10, v15, v14
	v_fmac_f32_e32 v15, v16, v12
	v_fma_f32 v10, -v10, v15, v14
	v_div_fmas_f32 v10, v10, v12, v15
	v_div_fixup_f32 v9, v10, v9, 1.0
